# L1: shape/color id loads for the self term prefetched at task start; L2: batch_vec prefetched
# speedup vs baseline: 1.0008x; 1.0008x over previous
.Lp1_after_idx:
	v_lshlrev_b32_e32 v114, 2, v94
	s_mov_b64 s[6:7], exec
	s_and_b64 exec, exec, s[4:5]
	global_load_dword v115, v114, s[14:15]
	global_load_dword v114, v114, s[16:17]
	s_mov_b64 exec, s[6:7]
	s_waitcnt vmcnt(0)
	v_lshrrev_b32_e32 v36, 10, v36
	v_lshrrev_b32_e32 v68, 10, v68
	v_lshrrev_b32_e32 v74, 10, v74
	v_lshrrev_b32_e32 v85, 10, v85
	v_lshrrev_b32_e32 v84, 10, v84
	v_lshrrev_b32_e32 v109, 10, v109
	v_lshrrev_b32_e32 v107, 10, v107
	v_lshrrev_b32_e32 v106, 10, v106
	v_lshrrev_b32_e32 v95, 10, v95
	v_and_b32_e32 v36, 0x3fff80, v36
	v_and_b32_e32 v68, 0x3fff80, v68
	v_and_b32_e32 v74, 0x3fff80, v74
	v_and_b32_e32 v85, 0x3fff80, v85
	v_and_b32_e32 v84, 0x3fff80, v84
	v_and_b32_e32 v109, 0x3fff80, v109
	v_and_b32_e32 v107, 0x3fff80, v107
	v_and_b32_e32 v106, 0x3fff80, v106
	v_and_b32_e32 v95, 0x3fff80, v95
	v_mov_b32_dpp v41, v36 row_newbcast:6 row_mask:0xf bank_mask:0x3
	v_mov_b32_dpp v41, v36 row_newbcast:14 row_mask:0xf bank_mask:0xc
	v_add_u32_dpp v37, v36, v102 row_newbcast:0 row_mask:0xf bank_mask:0x3
	v_add_u32_dpp v37, v36, v102 row_newbcast:8 row_mask:0xf bank_mask:0xc
	v_add_u32_dpp v38, v36, v102 row_newbcast:1 row_mask:0xf bank_mask:0x3
	v_add_u32_dpp v38, v36, v102 row_newbcast:9 row_mask:0xf bank_mask:0xc
	ds_read_b128 v[60:63], v37 offset:52240
	ds_read_b128 v[52:55], v38 offset:52240
	v_add_u32_dpp v37, v36, v102 row_newbcast:2 row_mask:0xf bank_mask:0x3
	v_add_u32_dpp v37, v36, v102 row_newbcast:10 row_mask:0xf bank_mask:0xc
	v_add_u32_dpp v39, v36, v102 row_newbcast:3 row_mask:0xf bank_mask:0x3
	v_add_u32_dpp v39, v36, v102 row_newbcast:11 row_mask:0xf bank_mask:0xc
	v_mov_b32_dpp v40, v36 row_newbcast:5 row_mask:0xf bank_mask:0x3
	v_mov_b32_dpp v40, v36 row_newbcast:13 row_mask:0xf bank_mask:0xc
	v_mov_b32_dpp v42, v36 row_newbcast:7 row_mask:0xf bank_mask:0x3
	v_mov_b32_dpp v42, v36 row_newbcast:15 row_mask:0xf bank_mask:0xc
	ds_read_b128 v[64:67], v37 offset:52240
	ds_read_b128 v[56:59], v39 offset:52240
	v_add_u32_dpp v37, v36, v102 row_newbcast:4 row_mask:0xf bank_mask:0x3
	v_add_u32_dpp v37, v36, v102 row_newbcast:12 row_mask:0xf bank_mask:0xc
	v_cmp_lt_i32_e32 vcc, 8, v72
	v_add_u32_e32 v36, v102, v40
	v_add_u32_e32 v40, v102, v41
	v_add_u32_e32 v41, v102, v42
	ds_read_b128 v[44:47], v37 offset:52240
	ds_read_b128 v[36:39], v36 offset:52240
	ds_read_b128 v[48:51], v40 offset:52240
	ds_read_b128 v[40:43], v41 offset:52240
	s_cmp_lg_u64 vcc, 0
	s_cselect_b64 s[22:23], -1, 0
	v_cmp_lt_i32_e64 s[6:7], 12, v72
	s_cbranch_vccz .LBB4_44
	v_add_u32_dpp v0, v68, v102 row_newbcast:0 row_mask:0xf bank_mask:0x3
	v_add_u32_dpp v0, v68, v102 row_newbcast:8 row_mask:0xf bank_mask:0xc
	v_add_u32_dpp v8, v68, v102 row_newbcast:1 row_mask:0xf bank_mask:0x3
	v_add_u32_dpp v8, v68, v102 row_newbcast:9 row_mask:0xf bank_mask:0xc
	v_add_u32_dpp v16, v68, v102 row_newbcast:2 row_mask:0xf bank_mask:0x3
	v_add_u32_dpp v16, v68, v102 row_newbcast:10 row_mask:0xf bank_mask:0xc
	v_add_u32_dpp v24, v68, v102 row_newbcast:3 row_mask:0xf bank_mask:0x3
	v_add_u32_dpp v24, v68, v102 row_newbcast:11 row_mask:0xf bank_mask:0xc
	ds_read_b128 v[0:3], v0 offset:52240
	ds_read_b128 v[8:11], v8 offset:52240
	ds_read_b128 v[16:19], v16 offset:52240
	ds_read_b128 v[24:27], v24 offset:52240

.LBB4_99:
	ds_write_b128 v104, v[68:71] offset:33792
	ds_read_b128 v[32:35], v105 offset:256
	ds_read_b128 v[52:55], v103 offset:33792
	ds_read_b128 v[56:59], v105 offset:8704
	s_waitcnt lgkmcnt(1)
	v_mfma_f32_16x16x32_f16 v[32:35], v[32:35], v[52:55], v[36:39]
	s_nop 2
	ds_read_b128 v[36:39], v105 offset:17152
	s_waitcnt lgkmcnt(1)
	v_mfma_f32_16x16x32_f16 v[40:43], v[56:59], v[52:55], v[40:43]
	s_waitcnt lgkmcnt(0)
	v_mfma_f32_16x16x32_f16 v[44:47], v[36:39], v[52:55], v[44:47]
	ds_read_b128 v[36:39], v105 offset:25600
	s_waitcnt lgkmcnt(0)
	v_mfma_f32_16x16x32_f16 v[52:55], v[36:39], v[52:55], v[48:51]
	ds_read_b128 v[36:39], v105 offset:320
	ds_read_b128 v[56:59], v103 offset:33856
	s_nop 0
	ds_read_b128 v[48:51], v105 offset:8768
	ds_read_b128 v[60:63], v105 offset:17216
	ds_read_b128 v[64:67], v105 offset:25664
	s_waitcnt lgkmcnt(3)
	v_mfma_f32_16x16x32_f16 v[32:35], v[36:39], v[56:59], v[32:35]
	s_waitcnt lgkmcnt(2)
	v_mfma_f32_16x16x32_f16 v[36:39], v[48:51], v[56:59], v[40:43]
	v_mov_b32_e32 v48, 0
	v_mov_b32_e32 v49, v48
	v_mov_b32_e32 v50, v48
	s_waitcnt lgkmcnt(1)
	v_mfma_f32_16x16x32_f16 v[40:43], v[60:63], v[56:59], v[44:47]
	v_mov_b32_e32 v51, v48
	s_waitcnt lgkmcnt(0)
	v_mfma_f32_16x16x32_f16 v[44:47], v[64:67], v[56:59], v[52:55]
	s_and_saveexec_b64 s[6:7], s[4:5]
	s_cbranch_execz .LBB4_101
	v_lshlrev_b32_e32 v48, 7, v114
	v_lshl_add_u32 v49, v115, 11, 0
	v_add3_u32 v48, v49, v48, v98
	ds_read_b128 v[48:51], v48 offset:52240

	.amdhsa_kernel _Z7k_layerILi1EEvPKDF16_PKiPKjS3_S3_S1_PKfPDF16_PhS3_S7_Pf
		.amdhsa_group_segment_fixed_size 256
		.amdhsa_private_segment_fixed_size 0
		.amdhsa_kernarg_size 352
		.amdhsa_user_sgpr_count 2
		.amdhsa_user_sgpr_dispatch_ptr 0
		.amdhsa_user_sgpr_queue_ptr 0
		.amdhsa_user_sgpr_kernarg_segment_ptr 1
		.amdhsa_user_sgpr_dispatch_id 0
		.amdhsa_user_sgpr_kernarg_preload_length 0
		.amdhsa_user_sgpr_kernarg_preload_offset 0
		.amdhsa_user_sgpr_private_segment_size 0
		.amdhsa_uses_dynamic_stack 0
		.amdhsa_enable_private_segment 0
		.amdhsa_system_sgpr_workgroup_id_x 1
		.amdhsa_system_sgpr_workgroup_id_y 0
		.amdhsa_system_sgpr_workgroup_id_z 0
		.amdhsa_system_sgpr_workgroup_info 0
		.amdhsa_system_vgpr_workitem_id 0
		.amdhsa_next_free_vgpr 116
		.amdhsa_next_free_sgpr 37
		.amdhsa_accum_offset 116
		.amdhsa_reserve_vcc 1
		.amdhsa_float_round_mode_32 0
		.amdhsa_float_round_mode_16_64 0
		.amdhsa_float_denorm_mode_32 3
		.amdhsa_float_denorm_mode_16_64 3
		.amdhsa_dx10_clamp 1
		.amdhsa_ieee_mode 1
		.amdhsa_fp16_overflow 0
		.amdhsa_tg_split 0
		.amdhsa_exception_fp_ieee_invalid_op 0
		.amdhsa_exception_fp_denorm_src 0
		.amdhsa_exception_fp_ieee_div_zero 0
		.amdhsa_exception_fp_ieee_overflow 0
		.amdhsa_exception_fp_ieee_underflow 0
		.amdhsa_exception_fp_ieee_inexact 0
		.amdhsa_exception_int_div_zero 0
	.end_amdhsa_kernel

.Lp2_after_idx:
	v_add_u32_e32 v102, s33, v77
	v_cmp_gt_i32_e32 vcc, s28, v102
	v_mov_b32_e32 v103, -1
	s_and_b64 s[8:9], s[2:3], vcc
	s_mov_b64 s[6:7], exec
	s_and_b64 exec, exec, s[8:9]
	v_lshlrev_b32_e32 v102, 2, v102
	global_load_dword v103, v102, s[16:17]
	s_mov_b64 exec, s[6:7]
	s_waitcnt vmcnt(0)
	v_lshlrev_b32_e32 v9, 6, v9
	v_lshlrev_b32_e32 v8, 6, v8
	v_lshlrev_b32_e32 v60, 6, v60
	v_lshlrev_b32_e32 v59, 6, v59
	v_lshlrev_b32_e32 v62, 6, v62
	v_lshlrev_b32_e32 v89, 6, v89
	v_lshlrev_b32_e32 v88, 6, v88
	v_lshlrev_b32_e32 v86, 6, v86
	v_lshlrev_b32_e32 v7, 6, v7
	v_and_b32_e32 v9, 0x7fffc0, v9
	v_and_b32_e32 v8, 0x7fffc0, v8
	v_and_b32_e32 v60, 0x7fffc0, v60
	v_and_b32_e32 v59, 0x7fffc0, v59
	v_and_b32_e32 v62, 0x7fffc0, v62
	v_and_b32_e32 v89, 0x7fffc0, v89
	v_and_b32_e32 v88, 0x7fffc0, v88
	v_and_b32_e32 v86, 0x7fffc0, v86
	v_and_b32_e32 v7, 0x7fffc0, v7
	v_mov_b32_dpp v12, v9 row_newbcast:2 row_mask:0xf bank_mask:0x3
	v_mov_b32_dpp v12, v9 row_newbcast:10 row_mask:0xf bank_mask:0xc
	v_mov_b32_dpp v14, v9 row_newbcast:4 row_mask:0xf bank_mask:0x3
	v_mov_b32_dpp v14, v9 row_newbcast:12 row_mask:0xf bank_mask:0xc
	v_mov_b32_dpp v15, v9 row_newbcast:5 row_mask:0xf bank_mask:0x3
	v_mov_b32_dpp v15, v9 row_newbcast:13 row_mask:0xf bank_mask:0xc
	v_add_u32_dpp v10, v9, v81 row_newbcast:0 row_mask:0xf bank_mask:0x3
	v_add_u32_dpp v10, v9, v81 row_newbcast:8 row_mask:0xf bank_mask:0xc
	v_add_u32_dpp v11, v9, v81 row_newbcast:1 row_mask:0xf bank_mask:0x3
	v_add_u32_dpp v11, v9, v81 row_newbcast:9 row_mask:0xf bank_mask:0xc
	v_add_u32_dpp v13, v9, v81 row_newbcast:3 row_mask:0xf bank_mask:0x3
	v_add_u32_dpp v13, v9, v81 row_newbcast:11 row_mask:0xf bank_mask:0xc
	v_mov_b32_dpp v16, v9 row_newbcast:6 row_mask:0xf bank_mask:0x3
	v_mov_b32_dpp v16, v9 row_newbcast:14 row_mask:0xf bank_mask:0xc
	v_mov_b32_dpp v9, v9 row_newbcast:7 row_mask:0xf bank_mask:0x3
	v_mov_b32_dpp v9, v9 row_newbcast:15 row_mask:0xf bank_mask:0xc
	v_add_u32_e32 v12, v12, v81
	global_load_dwordx2 v[56:57], v10, s[30:31]
	global_load_dwordx2 v[52:53], v11, s[30:31]
	global_load_dwordx2 v[30:31], v12, s[30:31]
	global_load_dwordx2 v[24:25], v13, s[30:31]
	v_add_u32_e32 v10, v14, v81
	v_add_u32_e32 v11, v15, v81
	v_add_u32_e32 v9, v9, v81
	v_add_u32_e32 v12, v16, v81
	v_mov_b32_dpp v16, v8 row_newbcast:3 row_mask:0xf bank_mask:0x3
	v_mov_b32_dpp v16, v8 row_newbcast:11 row_mask:0xf bank_mask:0xc
	global_load_dwordx2 v[54:55], v10, s[30:31]
	global_load_dwordx2 v[50:51], v11, s[30:31]
	global_load_dwordx2 v[26:27], v12, s[30:31]
	global_load_dwordx2 v[20:21], v9, s[30:31]
	v_add_u32_dpp v9, v8, v81 row_newbcast:0 row_mask:0xf bank_mask:0x3
	v_add_u32_dpp v9, v8, v81 row_newbcast:8 row_mask:0xf bank_mask:0xc
	v_add_u32_dpp v10, v8, v81 row_newbcast:1 row_mask:0xf bank_mask:0x3
	v_add_u32_dpp v10, v8, v81 row_newbcast:9 row_mask:0xf bank_mask:0xc
	v_add_u32_dpp v11, v8, v81 row_newbcast:2 row_mask:0xf bank_mask:0x3
	v_add_u32_dpp v11, v8, v81 row_newbcast:10 row_mask:0xf bank_mask:0xc
	v_mov_b32_dpp v13, v8 row_newbcast:4 row_mask:0xf bank_mask:0x3
	v_mov_b32_dpp v13, v8 row_newbcast:12 row_mask:0xf bank_mask:0xc
	v_mov_b32_dpp v14, v8 row_newbcast:5 row_mask:0xf bank_mask:0x3
	v_mov_b32_dpp v14, v8 row_newbcast:13 row_mask:0xf bank_mask:0xc
	v_mov_b32_dpp v15, v8 row_newbcast:6 row_mask:0xf bank_mask:0x3
	v_mov_b32_dpp v15, v8 row_newbcast:14 row_mask:0xf bank_mask:0xc
	v_mov_b32_dpp v8, v8 row_newbcast:7 row_mask:0xf bank_mask:0x3
	v_mov_b32_dpp v8, v8 row_newbcast:15 row_mask:0xf bank_mask:0xc
	v_add_u32_e32 v12, v16, v81
	global_load_dwordx2 v[28:29], v9, s[30:31]
	global_load_dwordx2 v[22:23], v10, s[30:31]
	global_load_dwordx2 v[18:19], v11, s[30:31]
	global_load_dwordx2 v[16:17], v12, s[30:31]
	v_add_u32_e32 v9, v13, v81
	v_add_u32_e32 v10, v14, v81
	v_add_u32_e32 v11, v15, v81
	v_add_u32_e32 v8, v8, v81
	global_load_dwordx2 v[14:15], v9, s[30:31]
	global_load_dwordx2 v[12:13], v10, s[30:31]
	s_nop 0
	global_load_dwordx2 v[10:11], v11, s[30:31]
	s_nop 0
	global_load_dwordx2 v[8:9], v8, s[30:31]
	v_cmp_lt_i32_e32 vcc, 16, v58
	s_cmp_lg_u64 vcc, 0
	s_cselect_b64 s[36:37], -1, 0
	v_cmp_lt_i32_e64 s[10:11], 18, v58
	v_cmp_lt_i32_e64 s[8:9], 20, v58
	v_cmp_lt_i32_e64 s[6:7], 22, v58
	s_cbranch_vccz .LBB5_42
	v_add_u32_dpp v34, v60, v81 row_newbcast:0 row_mask:0xf bank_mask:0x3
	v_add_u32_dpp v34, v60, v81 row_newbcast:8 row_mask:0xf bank_mask:0xc
	v_add_u32_dpp v38, v60, v81 row_newbcast:1 row_mask:0xf bank_mask:0x3
	v_add_u32_dpp v38, v60, v81 row_newbcast:9 row_mask:0xf bank_mask:0xc
	global_load_dwordx2 v[34:35], v34, s[30:31]
	s_nop 0
	global_load_dwordx2 v[38:39], v38, s[30:31]

.LBB5_105:
	s_cbranch_execz .LBB5_102
	ds_write_b128 v82, v[4:7] offset:33792
	ds_read_b128 v[4:7], v83 offset:256
	ds_read_b128 v[24:27], v80 offset:33792
	ds_read_b128 v[28:31], v83 offset:8704
	s_waitcnt lgkmcnt(1)
	v_mfma_f32_16x16x32_f16 v[4:7], v[4:7], v[24:27], v[8:11]
	s_nop 2
	ds_read_b128 v[8:11], v83 offset:17152
	s_waitcnt lgkmcnt(1)
	v_mfma_f32_16x16x32_f16 v[12:15], v[28:31], v[24:27], v[12:15]
	s_waitcnt lgkmcnt(0)
	v_mfma_f32_16x16x32_f16 v[8:11], v[8:11], v[24:27], v[16:19]
	s_nop 2
	ds_read_b128 v[16:19], v83 offset:25600
	s_waitcnt lgkmcnt(0)
	v_mfma_f32_16x16x32_f16 v[16:19], v[16:19], v[24:27], v[20:23]
	s_nop 2
	ds_read_b128 v[20:23], v83 offset:320
	ds_read_b128 v[24:27], v80 offset:33856
	ds_read_b128 v[28:31], v83 offset:8768
	s_waitcnt lgkmcnt(1)
	v_mfma_f32_16x16x32_f16 v[4:7], v[20:23], v[24:27], v[4:7]
	ds_read_b128 v[20:23], v83 offset:17216
	s_waitcnt lgkmcnt(1)
	v_mfma_f32_16x16x32_f16 v[12:15], v[28:31], v[24:27], v[12:15]
	s_waitcnt lgkmcnt(0)
	v_mfma_f32_16x16x32_f16 v[8:11], v[20:23], v[24:27], v[8:11]
	ds_read_b128 v[20:23], v83 offset:25664
	ds_write_b128 v82, v[0:3] offset:33792
	s_waitcnt lgkmcnt(1)
	v_mfma_f32_16x16x32_f16 v[0:3], v[20:23], v[24:27], v[16:19]
	s_nop 2
	ds_read_b128 v[16:19], v83 offset:384
	ds_read_b128 v[20:23], v80 offset:33792
	ds_read_b128 v[24:27], v83 offset:8832
	s_waitcnt lgkmcnt(1)
	v_mfma_f32_16x16x32_f16 v[4:7], v[16:19], v[20:23], v[4:7]
	ds_read_b128 v[16:19], v83 offset:17280
	s_waitcnt lgkmcnt(1)
	v_mfma_f32_16x16x32_f16 v[12:15], v[24:27], v[20:23], v[12:15]
	s_waitcnt lgkmcnt(0)
	v_mfma_f32_16x16x32_f16 v[8:11], v[16:19], v[20:23], v[8:11]
	ds_read_b128 v[16:19], v83 offset:25728
	s_waitcnt lgkmcnt(0)
	v_mfma_f32_16x16x32_f16 v[0:3], v[16:19], v[20:23], v[0:3]
	ds_read_b128 v[16:19], v83 offset:448
	ds_read_b128 v[20:23], v80 offset:33856
	ds_read_b128 v[24:27], v83 offset:8896
	ds_read_b128 v[28:31], v83 offset:17344
	ds_read_b128 v[50:53], v83 offset:25792
	s_mov_b64 s[6:7], s[22:23]
	s_mov_b64 s[8:9], s[18:19]
	s_waitcnt lgkmcnt(1)
	v_mfma_f32_16x16x32_f16 v[8:11], v[28:31], v[20:23], v[8:11]
	s_nop 0
	s_waitcnt lgkmcnt(0)
	v_mfma_f32_16x16x32_f16 v[0:3], v[50:53], v[20:23], v[0:3]
	v_mfma_f32_16x16x32_f16 v[16:19], v[16:19], v[20:23], v[4:7]
	s_nop 2
	v_add_u32_e32 v6, s33, v77
	v_mfma_f32_16x16x32_f16 v[12:15], v[24:27], v[20:23], v[12:15]
	v_cmp_gt_i32_e32 vcc, s28, v6
	ds_read_b128 v[20:23], v32 offset:52240
	ds_read_b128 v[24:27], v32 offset:52496
	ds_read_b128 v[28:31], v32 offset:52752
	s_waitcnt lgkmcnt(2)
	v_add_f32_e32 v7, v16, v20
	s_waitcnt lgkmcnt(1)
	v_mov_b32_e32 v4, v24
	s_waitcnt lgkmcnt(0)
	v_mov_b32_e32 v5, v28
	v_add_f32_e32 v16, v17, v21
	v_add_f32_e32 v17, v18, v22
	v_add_f32_e32 v18, v19, v23
	v_max_f32_e32 v24, 0, v7
	v_max_f32_e32 v62, 0, v16
	v_max_f32_e32 v64, 0, v17
	v_max_f32_e32 v66, 0, v18
	ds_read_b128 v[16:19], v32 offset:52304
	ds_read_b128 v[20:23], v32 offset:52560
	ds_read_b128 v[50:53], v32 offset:52816
	s_waitcnt lgkmcnt(2)
	v_add_f32_e32 v7, v12, v16
	v_add_f32_e32 v12, v13, v17
	v_add_f32_e32 v13, v14, v18
	v_add_f32_e32 v14, v15, v19
	v_max_f32_e32 v68, 0, v7
	v_max_f32_e32 v70, 0, v12
	v_max_f32_e32 v72, 0, v13
	v_max_f32_e32 v86, 0, v14
	ds_read_b128 v[12:15], v32 offset:52368
	ds_read_b128 v[16:19], v32 offset:52624
	ds_read_b128 v[54:57], v32 offset:52880
	v_pk_fma_f32 v[88:89], v[4:5], v[24:25], 0 op_sel_hi:[1,0,0]
	v_mov_b32_e32 v28, v25
	v_mov_b32_e32 v24, v26
	v_mov_b32_e32 v25, v30
	v_mov_b32_e32 v30, v27
	s_waitcnt lgkmcnt(4)
	v_mov_b32_e32 v26, v20
	s_waitcnt lgkmcnt(3)
	v_mov_b32_e32 v27, v50
	v_mov_b32_e32 v50, v21
	v_mov_b32_e32 v20, v22
	v_mov_b32_e32 v21, v52
	v_mov_b32_e32 v52, v23
	v_pk_fma_f32 v[22:23], v[28:29], v[62:63], v[88:89] op_sel_hi:[1,0,1]
	v_mov_b32_e32 v4, v33
	v_pk_fma_f32 v[22:23], v[24:25], v[64:65], v[22:23] op_sel_hi:[1,0,1]
	v_mov_b32_e32 v5, v33
	v_pk_fma_f32 v[22:23], v[30:31], v[66:67], v[22:23] op_sel_hi:[1,0,1]
	s_waitcnt lgkmcnt(2)
	v_add_f32_e32 v7, v8, v12
	v_pk_fma_f32 v[22:23], v[26:27], v[68:69], v[22:23] op_sel_hi:[1,0,1]
	s_waitcnt lgkmcnt(1)
	v_mov_b32_e32 v8, v16
	v_pk_fma_f32 v[22:23], v[50:51], v[70:71], v[22:23] op_sel_hi:[1,0,1]
	v_add_f32_e32 v11, v11, v15
	v_pk_fma_f32 v[20:21], v[20:21], v[72:73], v[22:23] op_sel_hi:[1,0,1]
	v_add_f32_e32 v22, v9, v13
	v_pk_fma_f32 v[20:21], v[52:53], v[86:87], v[20:21] op_sel_hi:[1,0,1]
	v_add_f32_e32 v23, v10, v14
	s_waitcnt lgkmcnt(0)
	v_mov_b32_e32 v9, v54
	v_max_f32_e32 v10, 0, v7
	v_mov_b32_e32 v54, v17
	v_max_f32_e32 v14, 0, v22
	v_pk_fma_f32 v[8:9], v[8:9], v[10:11], v[20:21] op_sel_hi:[1,0,1]
	v_mov_b32_e32 v12, v18
	v_mov_b32_e32 v13, v56
	v_max_f32_e32 v16, 0, v23
	v_pk_fma_f32 v[8:9], v[54:55], v[14:15], v[8:9] op_sel_hi:[1,0,1]
	v_max_f32_e32 v22, 0, v11
	v_pk_fma_f32 v[8:9], v[12:13], v[16:17], v[8:9] op_sel_hi:[1,0,1]
	v_mov_b32_e32 v56, v19
	ds_read_b128 v[10:13], v32 offset:52432
	ds_read_b128 v[14:17], v32 offset:52688
	ds_read_b128 v[18:21], v32 offset:52944
	v_pk_fma_f32 v[22:23], v[56:57], v[22:23], v[8:9] op_sel_hi:[1,0,1]
	v_and_b32_e32 v24, 64, v84
	v_xor_b32_e32 v7, 16, v84
	v_add_u32_e32 v8, 64, v24
	v_cmp_lt_i32_e64 s[6:7], v7, v8
	s_and_b64 s[8:9], s[2:3], vcc
	s_waitcnt lgkmcnt(2)
	v_add_f32_e32 v9, v0, v10
	v_add_f32_e32 v11, v1, v11
	s_waitcnt lgkmcnt(1)
	v_mov_b32_e32 v0, v14
	s_waitcnt lgkmcnt(0)
	v_mov_b32_e32 v1, v18
	v_max_f32_e32 v10, 0, v9
	v_add_f32_e32 v24, v2, v12
	v_add_f32_e32 v13, v3, v13
	v_mov_b32_e32 v18, v15
	v_max_f32_e32 v12, 0, v11
	v_pk_fma_f32 v[0:1], v[0:1], v[10:11], v[22:23] op_sel_hi:[1,0,1]
	v_mov_b32_e32 v2, v16
	v_mov_b32_e32 v3, v20
	v_max_f32_e32 v14, 0, v24
	v_pk_fma_f32 v[0:1], v[18:19], v[12:13], v[0:1] op_sel_hi:[1,0,1]
	v_cndmask_b32_e64 v7, v84, v7, s[6:7]
	v_mov_b32_e32 v20, v17
	v_max_f32_e32 v16, 0, v13
	v_pk_fma_f32 v[0:1], v[2:3], v[14:15], v[0:1] op_sel_hi:[1,0,1]
	v_lshlrev_b32_e32 v7, 2, v7
	v_pk_fma_f32 v[0:1], v[20:21], v[16:17], v[0:1] op_sel_hi:[1,0,1]
	ds_bpermute_b32 v2, v7, v0
	ds_bpermute_b32 v3, v7, v1
	v_xor_b32_e32 v7, 32, v84
	v_cmp_lt_i32_e64 s[6:7], v7, v8
	v_mov_b32_e32 v10, -1
	s_waitcnt lgkmcnt(0)
	v_pk_add_f32 v[0:1], v[0:1], v[2:3]
	v_cndmask_b32_e64 v7, v84, v7, s[6:7]
	v_lshlrev_b32_e32 v7, 2, v7
	ds_bpermute_b32 v2, v7, v0
	ds_bpermute_b32 v3, v7, v1
	v_mov_b32_e32 v7, 0
	s_and_saveexec_b64 s[6:7], s[8:9]
	s_cbranch_execz .LBB5_108
	v_mov_b32_e32 v10, v103
	s_waitcnt lgkmcnt(0)
	v_pk_add_f32 v[4:5], v[0:1], v[2:3]
	v_mov_b32_e32 v7, 1.0

	.amdhsa_kernel _Z7k_layerILi2EEvPKDF16_PKiPKjS3_S3_S1_PKfPDF16_PhS3_S7_Pf
		.amdhsa_group_segment_fixed_size 768
		.amdhsa_private_segment_fixed_size 0
		.amdhsa_kernarg_size 352
		.amdhsa_user_sgpr_count 2
		.amdhsa_user_sgpr_dispatch_ptr 0
		.amdhsa_user_sgpr_queue_ptr 0
		.amdhsa_user_sgpr_kernarg_segment_ptr 1
		.amdhsa_user_sgpr_dispatch_id 0
		.amdhsa_user_sgpr_kernarg_preload_length 0
		.amdhsa_user_sgpr_kernarg_preload_offset 0
		.amdhsa_user_sgpr_private_segment_size 0
		.amdhsa_uses_dynamic_stack 0
		.amdhsa_enable_private_segment 0
		.amdhsa_system_sgpr_workgroup_id_x 1
		.amdhsa_system_sgpr_workgroup_id_y 0
		.amdhsa_system_sgpr_workgroup_id_z 0
		.amdhsa_system_sgpr_workgroup_info 0
		.amdhsa_system_vgpr_workitem_id 0
		.amdhsa_next_free_vgpr 104
		.amdhsa_next_free_sgpr 42
		.amdhsa_accum_offset 104
		.amdhsa_reserve_vcc 1
		.amdhsa_float_round_mode_32 0
		.amdhsa_float_round_mode_16_64 0
		.amdhsa_float_denorm_mode_32 3
		.amdhsa_float_denorm_mode_16_64 3
		.amdhsa_dx10_clamp 1
		.amdhsa_ieee_mode 1
		.amdhsa_fp16_overflow 0
		.amdhsa_tg_split 0
		.amdhsa_exception_fp_ieee_invalid_op 0
		.amdhsa_exception_fp_denorm_src 0
		.amdhsa_exception_fp_ieee_div_zero 0
		.amdhsa_exception_fp_ieee_overflow 0
		.amdhsa_exception_fp_ieee_underflow 0
		.amdhsa_exception_fp_ieee_inexact 0
		.amdhsa_exception_int_div_zero 0
	.end_amdhsa_kernel

amdhsa.kernels:
  - .agpr_count:     0
    .args:
      - .actual_access:  read_only
        .address_space:  global
        .offset:         0
        .size:           8
        .value_kind:     global_buffer
      - .actual_access:  read_only
        .address_space:  global
        .offset:         8
        .size:           8
        .value_kind:     global_buffer
      - .actual_access:  read_only
        .address_space:  global
        .offset:         16
        .size:           8
        .value_kind:     global_buffer
      - .actual_access:  read_only
        .address_space:  global
        .offset:         24
        .size:           8
        .value_kind:     global_buffer
      - .actual_access:  read_only
        .address_space:  global
        .offset:         32
        .size:           8
        .value_kind:     global_buffer
      - .actual_access:  read_only
        .address_space:  global
        .offset:         40
        .size:           8
        .value_kind:     global_buffer
      - .actual_access:  read_only
        .address_space:  global
        .offset:         48
        .size:           8
        .value_kind:     global_buffer
      - .actual_access:  read_only
        .address_space:  global
        .offset:         56
        .size:           8
        .value_kind:     global_buffer
      - .actual_access:  read_only
        .address_space:  global
        .offset:         64
        .size:           8
        .value_kind:     global_buffer
      - .actual_access:  read_only
        .address_space:  global
        .offset:         72
        .size:           8
        .value_kind:     global_buffer
      - .actual_access:  read_only
        .address_space:  global
        .offset:         80
        .size:           8
        .value_kind:     global_buffer
      - .actual_access:  read_only
        .address_space:  global
        .offset:         88
        .size:           8
        .value_kind:     global_buffer
      - .actual_access:  write_only
        .address_space:  global
        .offset:         96
        .size:           8
        .value_kind:     global_buffer
      - .actual_access:  write_only
        .address_space:  global
        .offset:         104
        .size:           8
        .value_kind:     global_buffer
      - .actual_access:  write_only
        .address_space:  global
        .offset:         112
        .size:           8
        .value_kind:     global_buffer
      - .actual_access:  write_only
        .address_space:  global
        .offset:         120
        .size:           8
        .value_kind:     global_buffer
      - .actual_access:  write_only
        .address_space:  global
        .offset:         128
        .size:           8
        .value_kind:     global_buffer
      - .actual_access:  write_only
        .address_space:  global
        .offset:         136
        .size:           8
        .value_kind:     global_buffer
      - .actual_access:  write_only
        .address_space:  global
        .offset:         144
        .size:           8
        .value_kind:     global_buffer
      - .actual_access:  write_only
        .address_space:  global
        .offset:         152
        .size:           8
        .value_kind:     global_buffer
      - .actual_access:  write_only
        .address_space:  global
        .offset:         160
        .size:           8
        .value_kind:     global_buffer
    .group_segment_fixed_size: 0
    .kernarg_segment_align: 8
    .kernarg_segment_size: 168
    .language:       OpenCL C
    .language_version:
      - 2
      - 0
    .max_flat_workgroup_size: 1024
    .name:           _Z6k_prepPKiS0_PKfS2_S2_S2_S2_S2_S2_S2_S2_S2_PDF16_S3_S3_PfS4_S4_PjS3_S5_
    .private_segment_fixed_size: 0
    .sgpr_count:     27
    .sgpr_spill_count: 0
    .symbol:         _Z6k_prepPKiS0_PKfS2_S2_S2_S2_S2_S2_S2_S2_S2_PDF16_S3_S3_PfS4_S4_PjS3_S5_.kd
    .uniform_work_group_size: 1
    .uses_dynamic_stack: false
    .vgpr_count:     61
    .vgpr_spill_count: 0
    .wavefront_size: 64
  - .agpr_count:     0
    .args:
      - .actual_access:  read_only
        .address_space:  global
        .offset:         0
        .size:           8
        .value_kind:     global_buffer
      - .actual_access:  read_only
        .address_space:  global
        .offset:         8
        .size:           8
        .value_kind:     global_buffer
      - .actual_access:  read_only
        .address_space:  global
        .offset:         16
        .size:           8
        .value_kind:     global_buffer
      - .actual_access:  write_only
        .address_space:  global
        .offset:         24
        .size:           8
        .value_kind:     global_buffer
      - .actual_access:  write_only
        .address_space:  global
        .offset:         32
        .size:           8
        .value_kind:     global_buffer
      - .actual_access:  write_only
        .address_space:  global
        .offset:         40
        .size:           8
        .value_kind:     global_buffer
      - .actual_access:  read_only
        .address_space:  global
        .offset:         48
        .size:           8
        .value_kind:     global_buffer
      - .actual_access:  read_only
        .address_space:  global
        .offset:         56
        .size:           8
        .value_kind:     global_buffer
      - .actual_access:  read_only
        .address_space:  global
        .offset:         64
        .size:           8
        .value_kind:     global_buffer
      - .actual_access:  read_only
        .address_space:  global
        .offset:         72
        .size:           8
        .value_kind:     global_buffer
      - .actual_access:  read_only
        .address_space:  global
        .offset:         80
        .size:           8
        .value_kind:     global_buffer
      - .actual_access:  read_only
        .address_space:  global
        .offset:         88
        .size:           8
        .value_kind:     global_buffer
      - .actual_access:  read_only
        .address_space:  global
        .offset:         96
        .size:           8
        .value_kind:     global_buffer
      - .actual_access:  read_only
        .address_space:  global
        .offset:         104
        .size:           8
        .value_kind:     global_buffer
      - .actual_access:  read_only
        .address_space:  global
        .offset:         112
        .size:           8
        .value_kind:     global_buffer
      - .actual_access:  read_only
        .address_space:  global
        .offset:         120
        .size:           8
        .value_kind:     global_buffer
      - .actual_access:  read_only
        .address_space:  global
        .offset:         128
        .size:           8
        .value_kind:     global_buffer
      - .actual_access:  write_only
        .address_space:  global
        .offset:         136
        .size:           8
        .value_kind:     global_buffer
      - .actual_access:  write_only
        .address_space:  global
        .offset:         144
        .size:           8
        .value_kind:     global_buffer
      - .actual_access:  write_only
        .address_space:  global
        .offset:         152
        .size:           8
        .value_kind:     global_buffer
      - .actual_access:  write_only
        .address_space:  global
        .offset:         160
        .size:           8
        .value_kind:     global_buffer
      - .actual_access:  write_only
        .address_space:  global
        .offset:         168
        .size:           8
        .value_kind:     global_buffer
    .group_segment_fixed_size: 1696
    .kernarg_segment_align: 8
    .kernarg_segment_size: 176
    .language:       OpenCL C
    .language_version:
      - 2
      - 0
    .max_flat_workgroup_size: 1024
    .name:           _Z11k_localsortPKiS0_S0_PjPtPiPKjPKfS7_S7_S7_S7_S7_S7_S7_S7_S7_PDF16_S8_S8_PfS9_
    .private_segment_fixed_size: 0
    .sgpr_count:     71
    .sgpr_spill_count: 0
    .symbol:         _Z11k_localsortPKiS0_S0_PjPtPiPKjPKfS7_S7_S7_S7_S7_S7_S7_S7_S7_PDF16_S8_S8_PfS9_.kd
    .uniform_work_group_size: 1
    .uses_dynamic_stack: false
    .vgpr_count:     95
    .vgpr_spill_count: 0
    .wavefront_size: 64
  - .agpr_count:     0
    .args:
      - .actual_access:  read_only
        .address_space:  global
        .offset:         0
        .size:           8
        .value_kind:     global_buffer
      - .actual_access:  read_only
        .address_space:  global
        .offset:         8
        .size:           8
        .value_kind:     global_buffer
      - .actual_access:  read_only
        .address_space:  global
        .offset:         16
        .size:           8
        .value_kind:     global_buffer
      - .actual_access:  write_only
        .address_space:  global
        .offset:         24
        .size:           8
        .value_kind:     global_buffer
      - .actual_access:  write_only
        .address_space:  global
        .offset:         32
        .size:           8
        .value_kind:     global_buffer
    .group_segment_fixed_size: 54144
    .kernarg_segment_align: 8
    .kernarg_segment_size: 40
    .language:       OpenCL C
    .language_version:
      - 2
      - 0
    .max_flat_workgroup_size: 1024
    .name:           _Z12k_bucketsortPKjPKtPKiPiPj
    .private_segment_fixed_size: 0
    .sgpr_count:     70
    .sgpr_spill_count: 0
    .symbol:         _Z12k_bucketsortPKjPKtPKiPiPj.kd
    .uniform_work_group_size: 1
    .uses_dynamic_stack: false
    .vgpr_count:     59
    .vgpr_spill_count: 0
    .wavefront_size: 64
  - .agpr_count:     0
    .args:
      - .actual_access:  read_only
        .address_space:  global
        .offset:         0
        .size:           8
        .value_kind:     global_buffer
      - .actual_access:  read_only
        .address_space:  global
        .offset:         8
        .size:           8
        .value_kind:     global_buffer
      - .actual_access:  write_only
        .address_space:  global
        .offset:         16
        .size:           8
        .value_kind:     global_buffer
    .group_segment_fixed_size: 0
    .kernarg_segment_align: 8
    .kernarg_segment_size: 24
    .language:       OpenCL C
    .language_version:
      - 2
      - 0
    .max_flat_workgroup_size: 256
    .name:           _Z7k_finalPKfS0_Pf
    .private_segment_fixed_size: 0
    .sgpr_count:     14
    .sgpr_spill_count: 0
    .symbol:         _Z7k_finalPKfS0_Pf.kd
    .uniform_work_group_size: 1
    .uses_dynamic_stack: false
    .vgpr_count:     10
    .vgpr_spill_count: 0
    .wavefront_size: 64
  - .agpr_count:     0
    .args:
      - .actual_access:  read_only
        .address_space:  global
        .offset:         0
        .size:           8
        .value_kind:     global_buffer
      - .actual_access:  read_only
        .address_space:  global
        .offset:         8
        .size:           8
        .value_kind:     global_buffer
      - .actual_access:  read_only
        .address_space:  global
        .offset:         16
        .size:           8
        .value_kind:     global_buffer
      - .actual_access:  read_only
        .address_space:  global
        .offset:         24
        .size:           8
        .value_kind:     global_buffer
      - .actual_access:  read_only
        .address_space:  global
        .offset:         32
        .size:           8
        .value_kind:     global_buffer
      - .actual_access:  read_only
        .address_space:  global
        .offset:         40
        .size:           8
        .value_kind:     global_buffer
      - .address_space:  global
        .offset:         48
        .size:           8
        .value_kind:     global_buffer
      - .actual_access:  write_only
        .address_space:  global
        .offset:         56
        .size:           8
        .value_kind:     global_buffer
      - .address_space:  global
        .offset:         64
        .size:           8
        .value_kind:     global_buffer
      - .actual_access:  read_only
        .address_space:  global
        .offset:         72
        .size:           8
        .value_kind:     global_buffer
      - .address_space:  global
        .offset:         80
        .size:           8
        .value_kind:     global_buffer
      - .actual_access:  read_only
        .address_space:  global
        .offset:         88
        .size:           8
        .value_kind:     global_buffer
      - .offset:         96
        .size:           4
        .value_kind:     hidden_block_count_x
      - .offset:         100
        .size:           4
        .value_kind:     hidden_block_count_y
      - .offset:         104
        .size:           4
        .value_kind:     hidden_block_count_z
      - .offset:         108
        .size:           2
        .value_kind:     hidden_group_size_x
      - .offset:         110
        .size:           2
        .value_kind:     hidden_group_size_y
      - .offset:         112
        .size:           2
        .value_kind:     hidden_group_size_z
      - .offset:         114
        .size:           2
        .value_kind:     hidden_remainder_x
      - .offset:         116
        .size:           2
        .value_kind:     hidden_remainder_y
      - .offset:         118
        .size:           2
        .value_kind:     hidden_remainder_z
      - .offset:         136
        .size:           8
        .value_kind:     hidden_global_offset_x
      - .offset:         144
        .size:           8
        .value_kind:     hidden_global_offset_y
      - .offset:         152
        .size:           8
        .value_kind:     hidden_global_offset_z
      - .offset:         160
        .size:           2
        .value_kind:     hidden_grid_dims
      - .offset:         216
        .size:           4
        .value_kind:     hidden_dynamic_lds_size
    .group_segment_fixed_size: 256
    .kernarg_segment_align: 8
    .kernarg_segment_size: 352
    .language:       OpenCL C
    .language_version:
      - 2
      - 0
    .max_flat_workgroup_size: 1024
    .name:           _Z7k_layerILi1EEvPKDF16_PKiPKjS3_S3_S1_PKfPDF16_PhS3_S7_Pf
    .private_segment_fixed_size: 0
    .sgpr_count:     43
    .sgpr_spill_count: 0
    .symbol:         _Z7k_layerILi1EEvPKDF16_PKiPKjS3_S3_S1_PKfPDF16_PhS3_S7_Pf.kd
    .uniform_work_group_size: 1
    .uses_dynamic_stack: false
    .vgpr_count:     116
    .vgpr_spill_count: 0
    .wavefront_size: 64
  - .agpr_count:     0
    .args:
      - .actual_access:  read_only
        .address_space:  global
        .offset:         0
        .size:           8
        .value_kind:     global_buffer
      - .actual_access:  read_only
        .address_space:  global
        .offset:         8
        .size:           8
        .value_kind:     global_buffer
      - .actual_access:  read_only
        .address_space:  global
        .offset:         16
        .size:           8
        .value_kind:     global_buffer
      - .actual_access:  read_only
        .address_space:  global
        .offset:         24
        .size:           8
        .value_kind:     global_buffer
      - .actual_access:  read_only
        .address_space:  global
        .offset:         32
        .size:           8
        .value_kind:     global_buffer
      - .actual_access:  read_only
        .address_space:  global
        .offset:         40
        .size:           8
        .value_kind:     global_buffer
      - .address_space:  global
        .offset:         48
        .size:           8
        .value_kind:     global_buffer
      - .actual_access:  read_only
        .address_space:  global
        .offset:         56
        .size:           8
        .value_kind:     global_buffer
      - .address_space:  global
        .offset:         64
        .size:           8
        .value_kind:     global_buffer
      - .actual_access:  read_only
        .address_space:  global
        .offset:         72
        .size:           8
        .value_kind:     global_buffer
      - .address_space:  global
        .offset:         80
        .size:           8
        .value_kind:     global_buffer
      - .address_space:  global
        .offset:         88
        .size:           8
        .value_kind:     global_buffer
      - .offset:         96
        .size:           4
        .value_kind:     hidden_block_count_x
      - .offset:         100
        .size:           4
        .value_kind:     hidden_block_count_y
      - .offset:         104
        .size:           4
        .value_kind:     hidden_block_count_z
      - .offset:         108
        .size:           2
        .value_kind:     hidden_group_size_x
      - .offset:         110
        .size:           2
        .value_kind:     hidden_group_size_y
      - .offset:         112
        .size:           2
        .value_kind:     hidden_group_size_z
      - .offset:         114
        .size:           2
        .value_kind:     hidden_remainder_x
      - .offset:         116
        .size:           2
        .value_kind:     hidden_remainder_y
      - .offset:         118
        .size:           2
        .value_kind:     hidden_remainder_z
      - .offset:         136
        .size:           8
        .value_kind:     hidden_global_offset_x
      - .offset:         144
        .size:           8
        .value_kind:     hidden_global_offset_y
      - .offset:         152
        .size:           8
        .value_kind:     hidden_global_offset_z
      - .offset:         160
        .size:           2
        .value_kind:     hidden_grid_dims
      - .offset:         216
        .size:           4
        .value_kind:     hidden_dynamic_lds_size
    .group_segment_fixed_size: 768
    .kernarg_segment_align: 8
    .kernarg_segment_size: 352
    .language:       OpenCL C
    .language_version:
      - 2
      - 0
    .max_flat_workgroup_size: 1024
    .name:           _Z7k_layerILi2EEvPKDF16_PKiPKjS3_S3_S1_PKfPDF16_PhS3_S7_Pf
    .private_segment_fixed_size: 0
    .sgpr_count:     48
    .sgpr_spill_count: 0
    .symbol:         _Z7k_layerILi2EEvPKDF16_PKiPKjS3_S3_S1_PKfPDF16_PhS3_S7_Pf.kd
    .uniform_work_group_size: 1
    .uses_dynamic_stack: false
    .vgpr_count:     104
    .vgpr_spill_count: 0
    .wavefront_size: 64
